# speedup vs baseline: 1.0716x; 1.0066x over previous
.LBB0_3:
	s_mov_b32 s8, 0xbffff
	v_cmp_lt_u32_e32 vcc, s8, v2
	s_and_saveexec_b64 s[8:9], vcc
	s_xor_b64 s[12:13], exec, s[8:9]
	s_cbranch_execz .LBB0_15
	s_load_dwordx4 s[8:11], s[0:1], 0x48
	s_mov_b32 s14, 0xeffff
	v_cmp_lt_u32_e32 vcc, s14, v2
	s_and_saveexec_b64 s[14:15], vcc
	s_xor_b64 s[14:15], exec, s[14:15]
	s_cbranch_execz .LBB0_8
	s_mov_b32 s16, 0x153010
	v_cmp_gt_u32_e32 vcc, s16, v2
	s_and_saveexec_b64 s[16:17], vcc
	s_cbranch_execz .LBB0_7
	v_mov_b32_e32 v0, 0xff100000
	v_lshl_add_u32 v0, v2, 4, v0
	v_mov_b32_e32 v2, -1
	s_waitcnt lgkmcnt(0)
	s_and_b32 s21, s11, 0xffff
	s_mov_b32 s23, 0x20000
	s_mov_b32 s22, 0x6b0100
	s_mov_b32 s20, s10
	v_mov_b32_e32 v3, v2
	v_mov_b32_e32 v4, v2
	v_mov_b32_e32 v5, v2
	s_mov_b64 s[24:25], exec
	s_mov_b32 s26, 0x5fffff
	v_cmp_lt_u32_e32 vcc, s26, v0
	s_and_b64 exec, exec, vcc
	s_cbranch_execz .Lprep_f1
	buffer_store_dwordx4 v[2:5], v0, s[20:23], 0 offen sc1
.Lprep_f1:
	s_mov_b64 exec, s[24:25]
	v_cmp_gt_u32_e32 vcc, 0x80000, v0
	v_add_u32_e32 v0, 0x630100, v0
	s_and_b64 exec, exec, vcc
	s_cbranch_execz .LBB0_7
	buffer_store_dwordx4 v[2:5], v0, s[20:23], 0 offen sc1

	.amdhsa_kernel _Z11prep_kernelPKfPKiS0_S0_S0_S0_PDF16_S3_S3_S3_Pc
		.amdhsa_group_segment_fixed_size 0
		.amdhsa_private_segment_fixed_size 0
		.amdhsa_kernarg_size 88
		.amdhsa_user_sgpr_count 2
		.amdhsa_user_sgpr_dispatch_ptr 0
		.amdhsa_user_sgpr_queue_ptr 0
		.amdhsa_user_sgpr_kernarg_segment_ptr 1
		.amdhsa_user_sgpr_dispatch_id 0
		.amdhsa_user_sgpr_kernarg_preload_length 0
		.amdhsa_user_sgpr_kernarg_preload_offset 0
		.amdhsa_user_sgpr_private_segment_size 0
		.amdhsa_uses_dynamic_stack 0
		.amdhsa_enable_private_segment 0
		.amdhsa_system_sgpr_workgroup_id_x 1
		.amdhsa_system_sgpr_workgroup_id_y 0
		.amdhsa_system_sgpr_workgroup_id_z 0
		.amdhsa_system_sgpr_workgroup_info 0
		.amdhsa_system_vgpr_workitem_id 0
		.amdhsa_next_free_vgpr 14
		.amdhsa_next_free_sgpr 27
		.amdhsa_accum_offset 16
		.amdhsa_reserve_vcc 1
		.amdhsa_float_round_mode_32 0
		.amdhsa_float_round_mode_16_64 0
		.amdhsa_float_denorm_mode_32 3
		.amdhsa_float_denorm_mode_16_64 3
		.amdhsa_dx10_clamp 1
		.amdhsa_ieee_mode 1
		.amdhsa_fp16_overflow 0
		.amdhsa_tg_split 0
		.amdhsa_exception_fp_ieee_invalid_op 0
		.amdhsa_exception_fp_denorm_src 0
		.amdhsa_exception_fp_ieee_div_zero 0
		.amdhsa_exception_fp_ieee_overflow 0
		.amdhsa_exception_fp_ieee_underflow 0
		.amdhsa_exception_fp_ieee_inexact 0
		.amdhsa_exception_int_div_zero 0
	.end_amdhsa_kernel

amdhsa.kernels:
  - .agpr_count:     0
    .args:
      - .actual_access:  read_only
        .address_space:  global
        .offset:         0
        .size:           8
        .value_kind:     global_buffer
      - .actual_access:  read_only
        .address_space:  global
        .offset:         8
        .size:           8
        .value_kind:     global_buffer
      - .actual_access:  read_only
        .address_space:  global
        .offset:         16
        .size:           8
        .value_kind:     global_buffer
      - .actual_access:  read_only
        .address_space:  global
        .offset:         24
        .size:           8
        .value_kind:     global_buffer
      - .actual_access:  read_only
        .address_space:  global
        .offset:         32
        .size:           8
        .value_kind:     global_buffer
      - .actual_access:  read_only
        .address_space:  global
        .offset:         40
        .size:           8
        .value_kind:     global_buffer
      - .address_space:  global
        .offset:         48
        .size:           8
        .value_kind:     global_buffer
      - .address_space:  global
        .offset:         56
        .size:           8
        .value_kind:     global_buffer
      - .address_space:  global
        .offset:         64
        .size:           8
        .value_kind:     global_buffer
      - .address_space:  global
        .offset:         72
        .size:           8
        .value_kind:     global_buffer
      - .address_space:  global
        .offset:         80
        .size:           8
        .value_kind:     global_buffer
    .group_segment_fixed_size: 0
    .kernarg_segment_align: 8
    .kernarg_segment_size: 88
    .language:       OpenCL C
    .language_version:
      - 2
      - 0
    .max_flat_workgroup_size: 256
    .name:           _Z11prep_kernelPKfPKiS0_S0_S0_S0_PDF16_S3_S3_S3_Pc
    .private_segment_fixed_size: 0
    .sgpr_count:     33
    .sgpr_spill_count: 0
    .symbol:         _Z11prep_kernelPKfPKiS0_S0_S0_S0_PDF16_S3_S3_S3_Pc.kd
    .uniform_work_group_size: 1
    .uses_dynamic_stack: false
    .vgpr_count:     14
    .vgpr_spill_count: 0
    .wavefront_size: 64
  - .agpr_count:     0
    .args:
      - .actual_access:  read_only
        .address_space:  global
        .offset:         0
        .size:           8
        .value_kind:     global_buffer
      - .address_space:  global
        .offset:         8
        .size:           8
        .value_kind:     global_buffer
    .group_segment_fixed_size: 0
    .kernarg_segment_align: 8
    .kernarg_segment_size: 16
    .language:       OpenCL C
    .language_version:
      - 2
      - 0
    .max_flat_workgroup_size: 256
    .name:           _Z7cvt_wfcPKfPDF16_
    .private_segment_fixed_size: 0
    .sgpr_count:     12
    .sgpr_spill_count: 0
    .symbol:         _Z7cvt_wfcPKfPDF16_.kd
    .uniform_work_group_size: 1
    .uses_dynamic_stack: false
    .vgpr_count:     12
    .vgpr_spill_count: 0
    .wavefront_size: 64
  - .agpr_count:     12
    .args:
      - .actual_access:  read_only
        .address_space:  global
        .offset:         0
        .size:           8
        .value_kind:     global_buffer
      - .actual_access:  read_only
        .address_space:  global
        .offset:         8
        .size:           8
        .value_kind:     global_buffer
      - .address_space:  global
        .offset:         16
        .size:           8
        .value_kind:     global_buffer
      - .address_space:  global
        .offset:         24
        .size:           8
        .value_kind:     global_buffer
      - .offset:         32
        .size:           4
        .value_kind:     by_value
    .group_segment_fixed_size: 0
    .kernarg_segment_align: 8
    .kernarg_segment_size: 36
    .language:       OpenCL C
    .language_version:
      - 2
      - 0
    .max_flat_workgroup_size: 256
    .name:           _Z9lstm_stepPKfS0_PDF16_Pfi
    .private_segment_fixed_size: 0
    .sgpr_count:     21
    .sgpr_spill_count: 0
    .symbol:         _Z9lstm_stepPKfS0_PDF16_Pfi.kd
    .uniform_work_group_size: 1
    .uses_dynamic_stack: false
    .vgpr_count:     88
    .vgpr_spill_count: 0
    .wavefront_size: 64
  - .agpr_count:     0
    .args:
      - .actual_access:  read_only
        .address_space:  global
        .offset:         0
        .size:           8
        .value_kind:     global_buffer
      - .actual_access:  read_only
        .address_space:  global
        .offset:         8
        .size:           8
        .value_kind:     global_buffer
      - .address_space:  global
        .offset:         16
        .size:           8
        .value_kind:     global_buffer
      - .address_space:  global
        .offset:         24
        .size:           8
        .value_kind:     global_buffer
      - .address_space:  global
        .offset:         32
        .size:           8
        .value_kind:     global_buffer
      - .actual_access:  read_only
        .address_space:  global
        .offset:         40
        .size:           8
        .value_kind:     global_buffer
      - .address_space:  global
        .offset:         48
        .size:           8
        .value_kind:     global_buffer
    .group_segment_fixed_size: 0
    .kernarg_segment_align: 8
    .kernarg_segment_size: 56
    .language:       OpenCL C
    .language_version:
      - 2
      - 0
    .max_flat_workgroup_size: 512
    .name:           _Z15lstm_persistentPKDF16_PKfPDF16_PjS4_S2_S3_
    .private_segment_fixed_size: 0
    .sgpr_count:     62
    .sgpr_spill_count: 0
    .symbol:         _Z15lstm_persistentPKDF16_PKfPDF16_PjS4_S2_S3_.kd
    .uniform_work_group_size: 1
    .uses_dynamic_stack: false
    .vgpr_count:     242
    .vgpr_spill_count: 0
    .wavefront_size: 64
  - .agpr_count:     0
    .args:
      - .address_space:  global
        .offset:         0
        .size:           8
        .value_kind:     global_buffer
      - .address_space:  global
        .offset:         8
        .size:           8
        .value_kind:     global_buffer
      - .address_space:  global
        .offset:         16
        .size:           8
        .value_kind:     global_buffer
      - .address_space:  global
        .offset:         24
        .size:           8
        .value_kind:     global_buffer
      - .address_space:  global
        .offset:         32
        .size:           8
        .value_kind:     global_buffer
      - .offset:         40
        .size:           4
        .value_kind:     hidden_block_count_x
      - .offset:         44
        .size:           4
        .value_kind:     hidden_block_count_y
      - .offset:         48
        .size:           4
        .value_kind:     hidden_block_count_z
      - .offset:         52
        .size:           2
        .value_kind:     hidden_group_size_x
      - .offset:         54
        .size:           2
        .value_kind:     hidden_group_size_y
      - .offset:         56
        .size:           2
        .value_kind:     hidden_group_size_z
      - .offset:         58
        .size:           2
        .value_kind:     hidden_remainder_x
      - .offset:         60
        .size:           2
        .value_kind:     hidden_remainder_y
      - .offset:         62
        .size:           2
        .value_kind:     hidden_remainder_z
      - .offset:         80
        .size:           8
        .value_kind:     hidden_global_offset_x
      - .offset:         88
        .size:           8
        .value_kind:     hidden_global_offset_y
      - .offset:         96
        .size:           8
        .value_kind:     hidden_global_offset_z
      - .offset:         104
        .size:           2
        .value_kind:     hidden_grid_dims
      - .offset:         160
        .size:           4
        .value_kind:     hidden_dynamic_lds_size
    .group_segment_fixed_size: 0
    .kernarg_segment_align: 8
    .kernarg_segment_size: 296
    .language:       OpenCL C
    .language_version:
      - 2
      - 0
    .max_flat_workgroup_size: 512
    .name:           _Z11gemm_8phaseILi0EEvPKDF16_S1_PfPKfS4_
    .private_segment_fixed_size: 0
    .sgpr_count:     59
    .sgpr_spill_count: 0
    .symbol:         _Z11gemm_8phaseILi0EEvPKDF16_S1_PfPKfS4_.kd
    .uniform_work_group_size: 1
    .uses_dynamic_stack: false
    .vgpr_count:     226
    .vgpr_spill_count: 0
    .wavefront_size: 64
  - .agpr_count:     0
    .args:
      - .address_space:  global
        .offset:         0
        .size:           8
        .value_kind:     global_buffer
      - .address_space:  global
        .offset:         8
        .size:           8
        .value_kind:     global_buffer
      - .address_space:  global
        .offset:         16
        .size:           8
        .value_kind:     global_buffer
      - .address_space:  global
        .offset:         24
        .size:           8
        .value_kind:     global_buffer
      - .address_space:  global
        .offset:         32
        .size:           8
        .value_kind:     global_buffer
      - .offset:         40
        .size:           4
        .value_kind:     hidden_block_count_x
      - .offset:         44
        .size:           4
        .value_kind:     hidden_block_count_y
      - .offset:         48
        .size:           4
        .value_kind:     hidden_block_count_z
      - .offset:         52
        .size:           2
        .value_kind:     hidden_group_size_x
      - .offset:         54
        .size:           2
        .value_kind:     hidden_group_size_y
      - .offset:         56
        .size:           2
        .value_kind:     hidden_group_size_z
      - .offset:         58
        .size:           2
        .value_kind:     hidden_remainder_x
      - .offset:         60
        .size:           2
        .value_kind:     hidden_remainder_y
      - .offset:         62
        .size:           2
        .value_kind:     hidden_remainder_z
      - .offset:         80
        .size:           8
        .value_kind:     hidden_global_offset_x
      - .offset:         88
        .size:           8
        .value_kind:     hidden_global_offset_y
      - .offset:         96
        .size:           8
        .value_kind:     hidden_global_offset_z
      - .offset:         104
        .size:           2
        .value_kind:     hidden_grid_dims
      - .offset:         160
        .size:           4
        .value_kind:     hidden_dynamic_lds_size
    .group_segment_fixed_size: 0
    .kernarg_segment_align: 8
    .kernarg_segment_size: 296
    .language:       OpenCL C
    .language_version:
      - 2
      - 0
    .max_flat_workgroup_size: 512
    .name:           _Z11gemm_8phaseILi1EEvPKDF16_S1_PfPKfS4_
    .private_segment_fixed_size: 0
    .sgpr_count:     44
    .sgpr_spill_count: 0
    .symbol:         _Z11gemm_8phaseILi1EEvPKDF16_S1_PfPKfS4_.kd
    .uniform_work_group_size: 1
    .uses_dynamic_stack: false
    .vgpr_count:     234
    .vgpr_spill_count: 0
    .wavefront_size: 64
